# speedup vs baseline: 1.0363x; 1.0131x over previous
_Z13gather_kernelPK15HIP_vector_typeIjLj2EEPKiPK6OvfRecPKDF16_PKfPDF16_:
	s_setprio 3
	s_lshr_b32 s3, s2, 2
	s_and_b32 s3, s3, 0x3ffffffe
	s_and_b32 s4, s2, 1
	s_or_b32 s3, s3, s4
	s_cmpk_gt_u32 s3, 0x186
	s_cbranch_scc1 .LBB1_156
	s_load_dwordx4 s[8:11], s[0:1], 0x0
	s_load_dwordx2 s[64:65], s[0:1], 0x20
	s_movk_i32 s4, 0x80
	s_lshl_b32 s12, s3, 4
	s_addk_i32 s12, 0x800
	v_lshrrev_b32_e32 v2, 6, v0
	v_cmp_gt_u32_e64 s[4:5], s4, v0
	v_lshlrev_b32_e32 v1, 2, v0
	v_readfirstlane_b32 s62, v2
	s_and_saveexec_b64 s[6:7], s[4:5]
	v_mov_b32_e32 v2, 0
	ds_write_b32 v1, v2 offset:10832
	s_or_b64 exec, exec, s[6:7]
	s_waitcnt lgkmcnt(0)
	v_cmp_gt_u32_e64 s[6:7], 64, v0
	s_and_saveexec_b64 s[12:13], s[6:7]
	v_mov_b32_e32 v2, 0
	ds_write_b32 v1, v2 offset:11856
	s_or_b64 exec, exec, s[12:13]
	s_mul_i32 s15, s3, 0x5000
	s_mul_hi_u32 s13, s3, 0x5000
	s_add_u32 s8, s8, s15
	s_addc_u32 s9, s9, s13
	v_lshlrev_b32_e32 v2, 3, v0
	v_mov_b32_e32 v3, 0
	v_lshl_add_u64 v[4:5], s[8:9], 0, v[2:3]
	s_movk_i32 s13, 0x1000
	global_load_dwordx2 v[20:21], v2, s[8:9]
	global_load_dwordx2 v[18:19], v2, s[8:9] offset:2048
	v_add_co_u32_e32 v2, vcc, s13, v4
	s_movk_i32 s13, 0x2000
	s_nop 0
	v_addc_co_u32_e32 v3, vcc, 0, v5, vcc
	v_add_co_u32_e32 v6, vcc, s13, v4
	s_movk_i32 s13, 0x3000
	s_nop 0
	v_addc_co_u32_e32 v7, vcc, 0, v5, vcc
	v_add_co_u32_e32 v24, vcc, s13, v4
	v_or_b32_e32 v23, 0x400, v0
	s_nop 0
	v_addc_co_u32_e32 v25, vcc, 0, v5, vcc
	v_lshlrev_b32_e32 v8, 3, v23
	v_or_b32_e32 v22, 0x800, v0
	v_add_co_u32_e32 v26, vcc, 0x4000, v4
	global_load_dwordx2 v[16:17], v[2:3], off
	global_load_dwordx2 v[14:15], v[2:3], off offset:2048
	global_load_dwordx2 v[12:13], v8, s[8:9]
	global_load_dwordx2 v[10:11], v[6:7], off offset:2048
	v_lshlrev_b32_e32 v28, 3, v22
	v_addc_co_u32_e32 v27, vcc, 0, v5, vcc
	global_load_dwordx2 v[8:9], v[24:25], off
	global_load_dwordx2 v[6:7], v[24:25], off offset:2048
	global_load_dwordx2 v[4:5], v28, s[8:9]
	global_load_dwordx2 v[2:3], v[26:27], off offset:2048
	s_lshl_b32 s51, s3, 4
	s_addk_i32 s51, 0x800
	s_load_dwordx4 s[36:39], s[10:11], s51 offset:0x0
	s_load_dword s33, s[10:11], 0x640
	s_load_dword s63, s[64:65], 0x0
	v_mov_b32_e32 v54, 1
	s_waitcnt lgkmcnt(0)
	s_barrier
	s_min_u32 s36, s36, 0x280
	s_min_u32 s37, s37, 0x280
	s_min_u32 s38, s38, 0x280
	s_min_u32 s39, s39, 0x280
	s_addk_i32 s37, 0x280
	s_addk_i32 s38, 0x500
	s_addk_i32 s39, 0x780
	s_cmp_ge_u32 s62, 2
	s_cselect_b32 s54, s37, s36
	s_cselect_b32 s59, s39, s38
	s_mov_b32 s52, s36
	s_mov_b32 s53, s36
	s_mov_b32 s55, s37
	s_mov_b32 s56, s37
	s_mov_b32 s57, s38
	s_mov_b32 s58, s38
	s_mov_b32 s60, s39
	s_mov_b32 s61, s39
	v_cmp_gt_i32_e32 vcc, s52, v0
	s_and_saveexec_b64 s[8:9], vcc
	s_waitcnt vmcnt(9)
	v_lshrrev_b32_e32 v33, 16, v20
	v_lshlrev_b32_e32 v53, 2, v33
	ds_add_rtn_u32 v43, v53, v54 offset:10832
	s_or_b64 exec, exec, s[8:9]
	v_or_b32_e32 v55, 0x100, v0
	v_cmp_gt_i32_e32 vcc, s53, v55
	s_and_saveexec_b64 s[8:9], vcc
	s_waitcnt vmcnt(8)
	v_lshrrev_b32_e32 v34, 16, v18
	v_lshlrev_b32_e32 v53, 2, v34
	ds_add_rtn_u32 v44, v53, v54 offset:10832
	s_or_b64 exec, exec, s[8:9]
	v_or_b32_e32 v55, 0x200, v0
	v_cmp_gt_i32_e32 vcc, s54, v55
	s_and_saveexec_b64 s[8:9], vcc
	s_waitcnt vmcnt(7)
	v_lshrrev_b32_e32 v35, 16, v16
	v_lshlrev_b32_e32 v53, 2, v35
	ds_add_rtn_u32 v45, v53, v54 offset:10832
	s_or_b64 exec, exec, s[8:9]
	v_or_b32_e32 v55, 0x300, v0
	v_cmp_gt_i32_e32 vcc, s55, v55
	s_and_saveexec_b64 s[8:9], vcc
	s_waitcnt vmcnt(6)
	v_lshrrev_b32_e32 v36, 16, v14
	v_lshlrev_b32_e32 v53, 2, v36
	ds_add_rtn_u32 v46, v53, v54 offset:10832
	s_or_b64 exec, exec, s[8:9]
	v_or_b32_e32 v55, 0x400, v0
	v_cmp_gt_i32_e32 vcc, s56, v55
	s_and_saveexec_b64 s[8:9], vcc
	s_waitcnt vmcnt(5)
	v_lshrrev_b32_e32 v37, 16, v12
	v_lshlrev_b32_e32 v53, 2, v37
	ds_add_rtn_u32 v47, v53, v54 offset:10832
	s_or_b64 exec, exec, s[8:9]
	v_or_b32_e32 v55, 0x500, v0
	v_cmp_gt_i32_e32 vcc, s57, v55
	s_and_saveexec_b64 s[8:9], vcc
	s_waitcnt vmcnt(4)
	v_lshrrev_b32_e32 v38, 16, v10
	v_lshlrev_b32_e32 v53, 2, v38
	ds_add_rtn_u32 v48, v53, v54 offset:10832
	s_or_b64 exec, exec, s[8:9]
	v_or_b32_e32 v55, 0x600, v0
	v_cmp_gt_i32_e32 vcc, s58, v55
	s_and_saveexec_b64 s[8:9], vcc
	s_waitcnt vmcnt(3)
	v_lshrrev_b32_e32 v39, 16, v8
	v_lshlrev_b32_e32 v53, 2, v39
	ds_add_rtn_u32 v49, v53, v54 offset:10832
	s_or_b64 exec, exec, s[8:9]
	v_or_b32_e32 v55, 0x700, v0
	v_cmp_gt_i32_e32 vcc, s59, v55
	s_and_saveexec_b64 s[8:9], vcc
	s_waitcnt vmcnt(2)
	v_lshrrev_b32_e32 v40, 16, v6
	v_lshlrev_b32_e32 v53, 2, v40
	ds_add_rtn_u32 v50, v53, v54 offset:10832
	s_or_b64 exec, exec, s[8:9]
	v_or_b32_e32 v55, 0x800, v0
	v_cmp_gt_i32_e32 vcc, s60, v55
	s_and_saveexec_b64 s[8:9], vcc
	s_waitcnt vmcnt(1)
	v_lshrrev_b32_e32 v41, 16, v4
	v_lshlrev_b32_e32 v53, 2, v41
	ds_add_rtn_u32 v51, v53, v54 offset:10832
	s_or_b64 exec, exec, s[8:9]
	v_or_b32_e32 v55, 0x900, v0
	v_cmp_gt_i32_e32 vcc, s61, v55
	s_and_saveexec_b64 s[8:9], vcc
	s_waitcnt vmcnt(0)
	v_lshrrev_b32_e32 v42, 16, v2
	v_lshlrev_b32_e32 v53, 2, v42
	ds_add_rtn_u32 v52, v53, v54 offset:10832
	s_or_b64 exec, exec, s[8:9]
	s_waitcnt lgkmcnt(0)
	v_cmp_gt_i32_e32 vcc, s52, v0
	v_lshl_or_b32 v56, v43, 8, v33
	s_nop 0
	v_cndmask_b32_e32 v32, -1, v56, vcc
	v_or_b32_e32 v55, 0x100, v0
	v_cmp_gt_i32_e32 vcc, s53, v55
	v_lshl_or_b32 v56, v44, 8, v34
	s_nop 0
	v_cndmask_b32_e32 v27, -1, v56, vcc
	v_or_b32_e32 v55, 0x200, v0
	v_cmp_gt_i32_e32 vcc, s54, v55
	v_lshl_or_b32 v56, v45, 8, v35
	s_nop 0
	v_cndmask_b32_e32 v31, -1, v56, vcc
	v_or_b32_e32 v55, 0x300, v0
	v_cmp_gt_i32_e32 vcc, s55, v55
	v_lshl_or_b32 v56, v46, 8, v36
	s_nop 0
	v_cndmask_b32_e32 v26, -1, v56, vcc
	v_or_b32_e32 v55, 0x400, v0
	v_cmp_gt_i32_e32 vcc, s56, v55
	v_lshl_or_b32 v56, v47, 8, v37
	s_nop 0
	v_cndmask_b32_e32 v30, -1, v56, vcc
	v_or_b32_e32 v55, 0x500, v0
	v_cmp_gt_i32_e32 vcc, s57, v55
	v_lshl_or_b32 v56, v48, 8, v38
	s_nop 0
	v_cndmask_b32_e32 v24, -1, v56, vcc
	v_or_b32_e32 v55, 0x600, v0
	v_cmp_gt_i32_e32 vcc, s58, v55
	v_lshl_or_b32 v56, v49, 8, v39
	s_nop 0
	v_cndmask_b32_e32 v29, -1, v56, vcc
	v_or_b32_e32 v55, 0x700, v0
	v_cmp_gt_i32_e32 vcc, s59, v55
	v_lshl_or_b32 v56, v50, 8, v40
	s_nop 0
	v_cndmask_b32_e32 v23, -1, v56, vcc
	v_or_b32_e32 v55, 0x800, v0
	v_cmp_gt_i32_e32 vcc, s60, v55
	v_lshl_or_b32 v56, v51, 8, v41
	s_nop 0
	v_cndmask_b32_e32 v28, -1, v56, vcc
	v_or_b32_e32 v55, 0x900, v0
	v_cmp_gt_i32_e32 vcc, s61, v55
	v_lshl_or_b32 v56, v52, 8, v42
	s_nop 0
	v_cndmask_b32_e32 v22, -1, v56, vcc

.LBB1_81:
	s_or_b64 exec, exec, s[24:25]
	s_setprio 2
	v_xor_b32_e32 v0, 3, v57
	v_lshl_or_b32 v57, v0, 5, v58
	s_waitcnt vmcnt(1)
	ds_read_b32 v4, v57 offset:11472
	s_mov_b32 s0, 0xc350
	v_add_u32_e32 v59, 0x2c50, v59
	s_waitcnt lgkmcnt(0)
	v_add_u32_e32 v58, s34, v4
	v_cmp_gt_i32_e32 vcc, s0, v58
	s_and_saveexec_b64 s[24:25], vcc
	s_cbranch_execz .LBB1_106
	v_lshl_or_b32 v0, v58, 7, v56
	global_load_dwordx4 v[0:3], v0, s[14:15]
	v_mov_b32_e32 v5, 0x2840
	v_lshl_add_u32 v4, v4, 2, v5
	ds_read2_b32 v[46:47], v4 offset1:1
	v_mov_b32_e32 v4, 0
	v_mov_b32_e32 v5, v4
	v_mov_b64_e32 v[44:45], v[4:5]
	v_mov_b64_e32 v[42:43], v[4:5]
	s_waitcnt lgkmcnt(0)
	v_cmp_lt_i32_e32 vcc, v46, v47
	v_mov_b64_e32 v[6:7], v[4:5]
	s_and_saveexec_b64 s[26:27], vcc
	s_cbranch_execz .LBB1_100
	v_mov_b32_e32 v6, v4
	v_mov_b32_e32 v7, v4
	v_mov_b32_e32 v5, v4
	v_mov_b64_e32 v[10:11], v[6:7]
	v_mov_b64_e32 v[14:15], v[6:7]
	v_mov_b64_e32 v[18:19], v[6:7]
	v_mov_b64_e32 v[22:23], v[6:7]
	v_mov_b64_e32 v[26:27], v[6:7]
	v_mov_b64_e32 v[30:31], v[6:7]
	v_mov_b64_e32 v[34:35], v[6:7]
	v_lshlrev_b32_e32 v60, 2, v46
	s_mov_b64 s[28:29], 0
	s_mov_b32 s20, 0x7fff80
	v_mov_b64_e32 v[8:9], v[4:5]
	v_mov_b64_e32 v[12:13], v[4:5]
	v_mov_b64_e32 v[16:17], v[4:5]
	v_mov_b64_e32 v[20:21], v[4:5]
	v_mov_b64_e32 v[24:25], v[4:5]
	v_mov_b64_e32 v[28:29], v[4:5]
	v_mov_b64_e32 v[32:33], v[4:5]
	v_mov_b32_e32 v42, v4
	v_mov_b32_e32 v43, v4
	v_mov_b32_e32 v44, v4
	v_mov_b32_e32 v45, v4
	s_branch .LBB1_85

.LBB1_106:
	s_or_b64 exec, exec, s[24:25]
	s_setprio 1
	ds_read_b32 v4, v59 offset:256
	s_mov_b32 s0, 0xc350
	v_add_u32_e32 v57, 0x2c50, v57
	s_waitcnt lgkmcnt(0)
	v_add_u32_e32 v58, s34, v4
	v_cmp_gt_i32_e32 vcc, s0, v58
	s_and_saveexec_b64 s[24:25], vcc
	s_cbranch_execz .LBB1_131
	v_lshl_or_b32 v0, v58, 7, v56
	global_load_dwordx4 v[0:3], v0, s[14:15]
	v_mov_b32_e32 v5, 0x2840
	v_lshl_add_u32 v4, v4, 2, v5
	ds_read2_b32 v[46:47], v4 offset1:1
	v_mov_b32_e32 v4, 0
	v_mov_b32_e32 v5, v4
	v_mov_b64_e32 v[44:45], v[4:5]
	v_mov_b64_e32 v[42:43], v[4:5]
	s_waitcnt lgkmcnt(0)
	v_cmp_lt_i32_e32 vcc, v46, v47
	v_mov_b64_e32 v[6:7], v[4:5]
	s_and_saveexec_b64 s[26:27], vcc
	s_cbranch_execz .LBB1_125
	v_mov_b32_e32 v6, v4
	v_mov_b32_e32 v7, v4
	v_mov_b32_e32 v5, v4
	v_mov_b64_e32 v[10:11], v[6:7]
	v_mov_b64_e32 v[14:15], v[6:7]
	v_mov_b64_e32 v[18:19], v[6:7]
	v_mov_b64_e32 v[22:23], v[6:7]
	v_mov_b64_e32 v[26:27], v[6:7]
	v_mov_b64_e32 v[30:31], v[6:7]
	v_mov_b64_e32 v[34:35], v[6:7]
	v_lshlrev_b32_e32 v59, 2, v46
	s_mov_b64 s[28:29], 0
	s_mov_b32 s20, 0x7fff80
	v_mov_b64_e32 v[8:9], v[4:5]
	v_mov_b64_e32 v[12:13], v[4:5]
	v_mov_b64_e32 v[16:17], v[4:5]
	v_mov_b64_e32 v[20:21], v[4:5]
	v_mov_b64_e32 v[24:25], v[4:5]
	v_mov_b64_e32 v[28:29], v[4:5]
	v_mov_b64_e32 v[32:33], v[4:5]
	v_mov_b32_e32 v42, v4
	v_mov_b32_e32 v43, v4
	v_mov_b32_e32 v44, v4
	v_mov_b32_e32 v45, v4
	s_branch .LBB1_110

.LBB1_131:
	s_or_b64 exec, exec, s[24:25]
	s_setprio 0
	ds_read_b32 v4, v57 offset:384
	s_mov_b32 s0, 0xc350
	s_waitcnt lgkmcnt(0)
	v_add_u32_e32 v57, s34, v4
	v_cmp_gt_i32_e32 vcc, s0, v57
	s_and_saveexec_b64 s[0:1], vcc
	s_cbranch_execz .LBB1_156
	v_lshl_or_b32 v0, v57, 7, v56
	global_load_dwordx4 v[0:3], v0, s[14:15]
	v_mov_b32_e32 v5, 0x2840
	v_lshl_add_u32 v4, v4, 2, v5
	ds_read2_b32 v[46:47], v4 offset1:1
	v_mov_b32_e32 v4, 0
	v_mov_b32_e32 v5, v4
	v_mov_b64_e32 v[44:45], v[4:5]
	v_mov_b64_e32 v[42:43], v[4:5]
	s_waitcnt lgkmcnt(0)
	v_cmp_lt_i32_e32 vcc, v46, v47
	v_mov_b64_e32 v[6:7], v[4:5]
	s_and_saveexec_b64 s[24:25], vcc
	s_cbranch_execz .LBB1_150
	v_mov_b32_e32 v6, v4
	v_mov_b32_e32 v7, v4
	v_mov_b32_e32 v5, v4
	v_mov_b64_e32 v[10:11], v[6:7]
	v_mov_b64_e32 v[14:15], v[6:7]
	v_mov_b64_e32 v[18:19], v[6:7]
	v_mov_b64_e32 v[22:23], v[6:7]
	v_mov_b64_e32 v[26:27], v[6:7]
	v_mov_b64_e32 v[30:31], v[6:7]
	v_mov_b64_e32 v[34:35], v[6:7]
	v_lshlrev_b32_e32 v58, 2, v46
	s_mov_b64 s[26:27], 0
	s_mov_b32 s20, 0x7fff80
	v_mov_b64_e32 v[8:9], v[4:5]
	v_mov_b64_e32 v[12:13], v[4:5]
	v_mov_b64_e32 v[16:17], v[4:5]
	v_mov_b64_e32 v[20:21], v[4:5]
	v_mov_b64_e32 v[24:25], v[4:5]
	v_mov_b64_e32 v[28:29], v[4:5]
	v_mov_b64_e32 v[32:33], v[4:5]
	v_mov_b32_e32 v42, v4
	v_mov_b32_e32 v43, v4
	v_mov_b32_e32 v44, v4
	v_mov_b32_e32 v45, v4
	s_branch .LBB1_135
